# NSA selected branch: per-element tile mask (96 VALU + 32 s_nop per tile) replaced by per-lane block bit applied to row max and exponent bias (2 v_cndmask), exact same values
# speedup vs baseline: 1.0085x; 1.0033x over previous
.LBB0_1732:
	v_bfe_u32 v1, v150, 1, 1
	v_cmp_ne_u32_e32 vcc, 0, v1
	s_cmp_lg_u64 vcc, 0
	s_cselect_b64 s[16:17], -1, 0
	s_cbranch_vccz .LBB0_1737
	ds_read_b128 v[68:71], v171 offset:49152
	ds_read_b128 v[84:87], v171 offset:57344
	ds_read_b128 v[178:181], v172 offset:49152
	s_cmp_eq_u32 s89, 1
	s_cselect_b64 s[14:15], -1, 0
	v_cndmask_b32_e64 v1, 64, v163, s[14:15]
	s_mov_b64 s[98:99], vcc
	v_cndmask_b32_e32 v1, 0, v1, vcc
	s_cmp_eq_u64 s[14:15], 0
	s_waitcnt lgkmcnt(2)
	v_mfma_f32_32x32x16_bf16 v[68:83], v[68:71], v[100:103], 0
	s_waitcnt lgkmcnt(0)
	v_mfma_f32_32x32x16_bf16 v[68:83], v[178:181], v[108:111], v[68:83]
	ds_read_b128 v[178:181], v172 offset:57344
	v_mfma_f32_32x32x16_bf16 v[84:99], v[84:87], v[100:103], 0
	s_waitcnt lgkmcnt(0)
	v_mfma_f32_32x32x16_bf16 v[84:99], v[178:181], v[108:111], v[84:99]
	ds_read_b128 v[178:181], v173 offset:49152
	s_waitcnt lgkmcnt(0)
	v_mfma_f32_32x32x16_bf16 v[68:83], v[178:181], v[116:119], v[68:83]
	ds_read_b128 v[178:181], v173 offset:57344
	s_waitcnt lgkmcnt(0)
	v_mfma_f32_32x32x16_bf16 v[84:99], v[178:181], v[116:119], v[84:99]
	ds_read_b128 v[178:181], v174 offset:49152
	s_waitcnt lgkmcnt(0)
	v_mfma_f32_32x32x16_bf16 v[68:83], v[178:181], v[124:127], v[68:83]
	ds_read_b128 v[178:181], v174 offset:57344
	s_waitcnt lgkmcnt(0)
	v_mfma_f32_32x32x16_bf16 v[84:99], v[178:181], v[124:127], v[84:99]
	ds_read_b128 v[178:181], v171 offset:49280
	s_waitcnt lgkmcnt(0)
	v_mfma_f32_32x32x16_bf16 v[68:83], v[178:181], v[104:107], v[68:83]
	ds_read_b128 v[178:181], v171 offset:57472
	s_waitcnt lgkmcnt(0)
	v_mfma_f32_32x32x16_bf16 v[84:99], v[178:181], v[104:107], v[84:99]
	ds_read_b128 v[178:181], v172 offset:49280
	s_waitcnt lgkmcnt(0)
	v_mfma_f32_32x32x16_bf16 v[68:83], v[178:181], v[112:115], v[68:83]
	ds_read_b128 v[178:181], v172 offset:57472
	s_waitcnt lgkmcnt(0)
	v_mfma_f32_32x32x16_bf16 v[84:99], v[178:181], v[112:115], v[84:99]
	ds_read_b128 v[178:181], v173 offset:49280
	s_waitcnt lgkmcnt(0)
	v_mfma_f32_32x32x16_bf16 v[68:83], v[178:181], v[120:123], v[68:83]
	ds_read_b128 v[178:181], v173 offset:57472
	s_waitcnt lgkmcnt(0)
	v_mfma_f32_32x32x16_bf16 v[84:99], v[178:181], v[120:123], v[84:99]
	ds_read_b128 v[178:181], v174 offset:49280
	s_waitcnt lgkmcnt(0)
	v_mfma_f32_32x32x16_bf16 v[68:83], v[178:181], v[128:131], v[68:83]
	ds_read_b128 v[178:181], v174 offset:57472
	s_waitcnt lgkmcnt(0)
	v_mfma_f32_32x32x16_bf16 v[84:99], v[178:181], v[128:131], v[84:99]
	s_cbranch_scc1 .LBB0_1735
	v_sub_u32_e32 v1, v1, v137
	v_cmp_lt_i32_e32 vcc, 0, v1
	s_nop 5
	v_cndmask_b32_e32 v68, v168, v68, vcc
	v_cmp_lt_i32_e32 vcc, 32, v1
	s_nop 1
	v_cndmask_b32_e32 v84, v168, v84, vcc
	v_cmp_lt_i32_e32 vcc, 1, v1
	s_nop 1
	v_cndmask_b32_e32 v69, v168, v69, vcc
	v_cmp_lt_i32_e32 vcc, 33, v1
	s_nop 1
	v_cndmask_b32_e32 v85, v168, v85, vcc
	v_cmp_lt_i32_e32 vcc, 2, v1
	s_nop 1
	v_cndmask_b32_e32 v70, v168, v70, vcc
	v_cmp_lt_i32_e32 vcc, 34, v1
	s_nop 1
	v_cndmask_b32_e32 v86, v168, v86, vcc
	v_cmp_lt_i32_e32 vcc, 3, v1
	s_nop 1
	v_cndmask_b32_e32 v71, v168, v71, vcc
	v_cmp_lt_i32_e32 vcc, 35, v1
	s_nop 1
	v_cndmask_b32_e32 v87, v168, v87, vcc
	v_cmp_lt_i32_e32 vcc, 8, v1
	s_nop 1
	v_cndmask_b32_e32 v72, v168, v72, vcc
	v_cmp_lt_i32_e32 vcc, 40, v1
	s_nop 1
	v_cndmask_b32_e32 v88, v168, v88, vcc
	v_cmp_lt_i32_e32 vcc, 9, v1
	s_nop 1
	v_cndmask_b32_e32 v73, v168, v73, vcc
	v_cmp_lt_i32_e32 vcc, 41, v1
	s_nop 1
	v_cndmask_b32_e32 v89, v168, v89, vcc
	v_cmp_lt_i32_e32 vcc, 10, v1
	s_nop 1
	v_cndmask_b32_e32 v74, v168, v74, vcc
	v_cmp_lt_i32_e32 vcc, 42, v1
	s_nop 1
	v_cndmask_b32_e32 v90, v168, v90, vcc
	v_cmp_lt_i32_e32 vcc, 11, v1
	s_nop 1
	v_cndmask_b32_e32 v75, v168, v75, vcc
	v_cmp_lt_i32_e32 vcc, 43, v1
	s_nop 1
	v_cndmask_b32_e32 v91, v168, v91, vcc
	v_cmp_lt_i32_e32 vcc, 16, v1
	s_nop 1
	v_cndmask_b32_e32 v76, v168, v76, vcc
	v_cmp_lt_i32_e32 vcc, 48, v1
	s_nop 1
	v_cndmask_b32_e32 v92, v168, v92, vcc
	v_cmp_lt_i32_e32 vcc, 17, v1
	s_nop 1
	v_cndmask_b32_e32 v77, v168, v77, vcc
	v_cmp_lt_i32_e32 vcc, 49, v1
	s_nop 1
	v_cndmask_b32_e32 v93, v168, v93, vcc
	v_cmp_lt_i32_e32 vcc, 18, v1
	s_nop 1
	v_cndmask_b32_e32 v78, v168, v78, vcc
	v_cmp_lt_i32_e32 vcc, 50, v1
	s_nop 1
	v_cndmask_b32_e32 v94, v168, v94, vcc
	v_cmp_lt_i32_e32 vcc, 19, v1
	s_nop 1
	v_cndmask_b32_e32 v79, v168, v79, vcc
	v_cmp_lt_i32_e32 vcc, 51, v1
	s_nop 1
	v_cndmask_b32_e32 v95, v168, v95, vcc
	v_cmp_lt_i32_e32 vcc, 24, v1
	s_nop 1
	v_cndmask_b32_e32 v80, v168, v80, vcc
	v_cmp_lt_i32_e32 vcc, 56, v1
	s_nop 1
	v_cndmask_b32_e32 v96, v168, v96, vcc
	v_cmp_lt_i32_e32 vcc, 25, v1
	s_nop 1
	v_cndmask_b32_e32 v81, v168, v81, vcc
	v_cmp_lt_i32_e32 vcc, 57, v1
	s_nop 1
	v_cndmask_b32_e32 v97, v168, v97, vcc
	v_cmp_lt_i32_e32 vcc, 26, v1
	s_nop 1
	v_cndmask_b32_e32 v82, v168, v82, vcc
	v_cmp_lt_i32_e32 vcc, 58, v1
	s_nop 1
	v_cndmask_b32_e32 v98, v168, v98, vcc
	v_cmp_lt_i32_e32 vcc, 27, v1
	s_nop 1
	v_cndmask_b32_e32 v83, v168, v83, vcc
	v_cmp_lt_i32_e32 vcc, 59, v1
	s_nop 1
	v_cndmask_b32_e32 v99, v168, v99, vcc
.LBB0_1735:
	s_nop 7
	v_max_f32_e32 v1, v69, v69
	v_max_f32_e32 v2, v68, v68
	v_max_f32_e32 v1, v2, v1
	v_max3_f32 v1, v1, v70, v71
	v_max3_f32 v1, v1, v72, v73
	v_max3_f32 v1, v1, v74, v75
	v_max3_f32 v1, v1, v76, v77
	v_max3_f32 v1, v1, v78, v79
	v_max3_f32 v1, v1, v80, v81
	v_max3_f32 v1, v1, v82, v83
	v_max3_f32 v1, v1, v84, v85
	v_max3_f32 v1, v1, v86, v87
	v_max3_f32 v1, v1, v88, v89
	v_max3_f32 v1, v1, v90, v91
	v_max3_f32 v1, v1, v92, v93
	v_max3_f32 v1, v1, v94, v95
	v_max3_f32 v1, v1, v96, v97
	v_max3_f32 v1, v1, v98, v99
	v_mov_b32_e32 v2, v1
	s_nop 1
	v_permlane32_swap_b32_e32 v1, v2
	v_max_f32_e32 v2, v2, v2
	v_max_f32_e32 v1, v1, v1
	v_max_f32_e32 v1, v1, v2
	v_cndmask_b32_e64 v1, v168, v1, s[98:99]
	v_sub_f32_e32 v2, v1, v175
	s_mov_b32 s1, 0x42b504f3
	v_cmp_ge_f32_e32 vcc, s1, v2
	s_cmp_eq_u64 vcc, exec
	v_mov_b32_e32 v178, 1.0
	s_cbranch_scc0 .LBB0_2102
.LBB0_1736:
	v_mul_f32_e32 v2, 0xbe0293ee, v175
	v_cndmask_b32_e64 v2, v168, v2, s[98:99]
	v_pk_fma_f32 v[68:69], v[68:69], s[2:3], v[2:3] op_sel_hi:[1,0,0]
	v_pk_fma_f32 v[70:71], v[70:71], s[2:3], v[2:3] op_sel_hi:[1,0,0]
	v_pk_fma_f32 v[72:73], v[72:73], s[2:3], v[2:3] op_sel_hi:[1,0,0]
	v_pk_fma_f32 v[74:75], v[74:75], s[2:3], v[2:3] op_sel_hi:[1,0,0]
	v_pk_fma_f32 v[76:77], v[76:77], s[2:3], v[2:3] op_sel_hi:[1,0,0]
	v_pk_fma_f32 v[78:79], v[78:79], s[2:3], v[2:3] op_sel_hi:[1,0,0]
	v_pk_fma_f32 v[80:81], v[80:81], s[2:3], v[2:3] op_sel_hi:[1,0,0]
	v_pk_fma_f32 v[82:83], v[82:83], s[2:3], v[2:3] op_sel_hi:[1,0,0]
	v_exp_f32_e32 v68, v68
	v_exp_f32_e32 v69, v69
	v_exp_f32_e32 v70, v70
	v_exp_f32_e32 v71, v71
	v_exp_f32_e32 v72, v72
	v_exp_f32_e32 v73, v73
	v_exp_f32_e32 v74, v74
	v_exp_f32_e32 v75, v75
	v_exp_f32_e32 v76, v76
	v_exp_f32_e32 v77, v77
	v_exp_f32_e32 v78, v78
	v_exp_f32_e32 v79, v79
	v_exp_f32_e32 v80, v80
	v_exp_f32_e32 v81, v81
	v_exp_f32_e32 v82, v82
	v_exp_f32_e32 v83, v83
	v_pk_fma_f32 v[86:87], v[86:87], s[2:3], v[2:3] op_sel_hi:[1,0,0]
	v_pk_fma_f32 v[84:85], v[84:85], s[2:3], v[2:3] op_sel_hi:[1,0,0]
	v_pk_fma_f32 v[88:89], v[88:89], s[2:3], v[2:3] op_sel_hi:[1,0,0]
	v_pk_fma_f32 v[90:91], v[90:91], s[2:3], v[2:3] op_sel_hi:[1,0,0]
	v_pk_fma_f32 v[92:93], v[92:93], s[2:3], v[2:3] op_sel_hi:[1,0,0]
	v_pk_fma_f32 v[94:95], v[94:95], s[2:3], v[2:3] op_sel_hi:[1,0,0]
	v_pk_fma_f32 v[96:97], v[96:97], s[2:3], v[2:3] op_sel_hi:[1,0,0]
	v_pk_fma_f32 v[98:99], v[98:99], s[2:3], v[2:3] op_sel_hi:[1,0,0]

.LBB0_1760:
	s_add_i32 s6, s1, s30
	s_cmp_lt_u32 s3, 32
	v_lshrrev_b32_e32 v1, s3, v150
	s_cselect_b64 s[12:13], -1, 0
	s_sub_i32 s3, s30, 35
	v_lshrrev_b32_e32 v2, s3, v151
	v_cndmask_b32_e64 v1, v2, v1, s[12:13]
	v_and_b32_e32 v1, 1, v1
	v_cmp_ne_u32_e32 vcc, 0, v1
	s_cmp_lg_u64 vcc, 0
	s_cselect_b64 s[20:21], -1, 0
	s_cbranch_vccz .LBB0_1765
	ds_read_b128 v[68:71], v171 offset:32768
	ds_read_b128 v[84:87], v171 offset:40960
	ds_read_b128 v[178:181], v172 offset:32768
	s_cmp_eq_u32 s6, 3
	s_cselect_b64 s[14:15], -1, 0
	v_cndmask_b32_e64 v1, 64, v163, s[14:15]
	s_mov_b64 s[98:99], vcc
	v_cndmask_b32_e32 v1, 0, v1, vcc
	s_cmp_eq_u64 s[14:15], 0
	s_waitcnt lgkmcnt(2)
	v_mfma_f32_32x32x16_bf16 v[68:83], v[68:71], v[100:103], 0
	s_waitcnt lgkmcnt(0)
	v_mfma_f32_32x32x16_bf16 v[68:83], v[178:181], v[108:111], v[68:83]
	ds_read_b128 v[178:181], v172 offset:40960
	v_mfma_f32_32x32x16_bf16 v[84:99], v[84:87], v[100:103], 0
	s_waitcnt lgkmcnt(0)
	v_mfma_f32_32x32x16_bf16 v[84:99], v[178:181], v[108:111], v[84:99]
	ds_read_b128 v[178:181], v173 offset:32768
	s_waitcnt lgkmcnt(0)
	v_mfma_f32_32x32x16_bf16 v[68:83], v[178:181], v[116:119], v[68:83]
	ds_read_b128 v[178:181], v173 offset:40960
	s_waitcnt lgkmcnt(0)
	v_mfma_f32_32x32x16_bf16 v[84:99], v[178:181], v[116:119], v[84:99]
	ds_read_b128 v[178:181], v174 offset:32768
	s_waitcnt lgkmcnt(0)
	v_mfma_f32_32x32x16_bf16 v[68:83], v[178:181], v[124:127], v[68:83]
	ds_read_b128 v[178:181], v174 offset:40960
	s_waitcnt lgkmcnt(0)
	v_mfma_f32_32x32x16_bf16 v[84:99], v[178:181], v[124:127], v[84:99]
	ds_read_b128 v[178:181], v171 offset:32896
	s_waitcnt lgkmcnt(0)
	v_mfma_f32_32x32x16_bf16 v[68:83], v[178:181], v[104:107], v[68:83]
	ds_read_b128 v[178:181], v171 offset:41088
	s_waitcnt lgkmcnt(0)
	v_mfma_f32_32x32x16_bf16 v[84:99], v[178:181], v[104:107], v[84:99]
	ds_read_b128 v[178:181], v172 offset:32896
	s_waitcnt lgkmcnt(0)
	v_mfma_f32_32x32x16_bf16 v[68:83], v[178:181], v[112:115], v[68:83]
	ds_read_b128 v[178:181], v172 offset:41088
	s_waitcnt lgkmcnt(0)
	v_mfma_f32_32x32x16_bf16 v[84:99], v[178:181], v[112:115], v[84:99]
	ds_read_b128 v[178:181], v173 offset:32896
	s_waitcnt lgkmcnt(0)
	v_mfma_f32_32x32x16_bf16 v[68:83], v[178:181], v[120:123], v[68:83]
	ds_read_b128 v[178:181], v173 offset:41088
	s_waitcnt lgkmcnt(0)
	v_mfma_f32_32x32x16_bf16 v[84:99], v[178:181], v[120:123], v[84:99]
	ds_read_b128 v[178:181], v174 offset:32896
	s_waitcnt lgkmcnt(0)
	v_mfma_f32_32x32x16_bf16 v[68:83], v[178:181], v[128:131], v[68:83]
	ds_read_b128 v[178:181], v174 offset:41088
	s_waitcnt lgkmcnt(0)
	v_mfma_f32_32x32x16_bf16 v[84:99], v[178:181], v[128:131], v[84:99]
	s_cbranch_scc1 .LBB0_1763
	v_sub_u32_e32 v1, v1, v137
	v_cmp_lt_i32_e32 vcc, 0, v1
	s_nop 5
	v_cndmask_b32_e32 v68, v168, v68, vcc
	v_cmp_lt_i32_e32 vcc, 32, v1
	s_nop 1
	v_cndmask_b32_e32 v84, v168, v84, vcc
	v_cmp_lt_i32_e32 vcc, 1, v1
	s_nop 1
	v_cndmask_b32_e32 v69, v168, v69, vcc
	v_cmp_lt_i32_e32 vcc, 33, v1
	s_nop 1
	v_cndmask_b32_e32 v85, v168, v85, vcc
	v_cmp_lt_i32_e32 vcc, 2, v1
	s_nop 1
	v_cndmask_b32_e32 v70, v168, v70, vcc
	v_cmp_lt_i32_e32 vcc, 34, v1
	s_nop 1
	v_cndmask_b32_e32 v86, v168, v86, vcc
	v_cmp_lt_i32_e32 vcc, 3, v1
	s_nop 1
	v_cndmask_b32_e32 v71, v168, v71, vcc
	v_cmp_lt_i32_e32 vcc, 35, v1
	s_nop 1
	v_cndmask_b32_e32 v87, v168, v87, vcc
	v_cmp_lt_i32_e32 vcc, 8, v1
	s_nop 1
	v_cndmask_b32_e32 v72, v168, v72, vcc
	v_cmp_lt_i32_e32 vcc, 40, v1
	s_nop 1
	v_cndmask_b32_e32 v88, v168, v88, vcc
	v_cmp_lt_i32_e32 vcc, 9, v1
	s_nop 1
	v_cndmask_b32_e32 v73, v168, v73, vcc
	v_cmp_lt_i32_e32 vcc, 41, v1
	s_nop 1
	v_cndmask_b32_e32 v89, v168, v89, vcc
	v_cmp_lt_i32_e32 vcc, 10, v1
	s_nop 1
	v_cndmask_b32_e32 v74, v168, v74, vcc
	v_cmp_lt_i32_e32 vcc, 42, v1
	s_nop 1
	v_cndmask_b32_e32 v90, v168, v90, vcc
	v_cmp_lt_i32_e32 vcc, 11, v1
	s_nop 1
	v_cndmask_b32_e32 v75, v168, v75, vcc
	v_cmp_lt_i32_e32 vcc, 43, v1
	s_nop 1
	v_cndmask_b32_e32 v91, v168, v91, vcc
	v_cmp_lt_i32_e32 vcc, 16, v1
	s_nop 1
	v_cndmask_b32_e32 v76, v168, v76, vcc
	v_cmp_lt_i32_e32 vcc, 48, v1
	s_nop 1
	v_cndmask_b32_e32 v92, v168, v92, vcc
	v_cmp_lt_i32_e32 vcc, 17, v1
	s_nop 1
	v_cndmask_b32_e32 v77, v168, v77, vcc
	v_cmp_lt_i32_e32 vcc, 49, v1
	s_nop 1
	v_cndmask_b32_e32 v93, v168, v93, vcc
	v_cmp_lt_i32_e32 vcc, 18, v1
	s_nop 1
	v_cndmask_b32_e32 v78, v168, v78, vcc
	v_cmp_lt_i32_e32 vcc, 50, v1
	s_nop 1
	v_cndmask_b32_e32 v94, v168, v94, vcc
	v_cmp_lt_i32_e32 vcc, 19, v1
	s_nop 1
	v_cndmask_b32_e32 v79, v168, v79, vcc
	v_cmp_lt_i32_e32 vcc, 51, v1
	s_nop 1
	v_cndmask_b32_e32 v95, v168, v95, vcc
	v_cmp_lt_i32_e32 vcc, 24, v1
	s_nop 1
	v_cndmask_b32_e32 v80, v168, v80, vcc
	v_cmp_lt_i32_e32 vcc, 56, v1
	s_nop 1
	v_cndmask_b32_e32 v96, v168, v96, vcc
	v_cmp_lt_i32_e32 vcc, 25, v1
	s_nop 1
	v_cndmask_b32_e32 v81, v168, v81, vcc
	v_cmp_lt_i32_e32 vcc, 57, v1
	s_nop 1
	v_cndmask_b32_e32 v97, v168, v97, vcc
	v_cmp_lt_i32_e32 vcc, 26, v1
	s_nop 1
	v_cndmask_b32_e32 v82, v168, v82, vcc
	v_cmp_lt_i32_e32 vcc, 58, v1
	s_nop 1
	v_cndmask_b32_e32 v98, v168, v98, vcc
	v_cmp_lt_i32_e32 vcc, 27, v1
	s_nop 1
	v_cndmask_b32_e32 v83, v168, v83, vcc
	v_cmp_lt_i32_e32 vcc, 59, v1
	s_nop 1
	v_cndmask_b32_e32 v99, v168, v99, vcc
.LBB0_1763:
	s_nop 7
	v_max_f32_e32 v1, v69, v69
	v_max_f32_e32 v2, v68, v68
	v_max_f32_e32 v1, v2, v1
	v_max3_f32 v1, v1, v70, v71
	v_max3_f32 v1, v1, v72, v73
	v_max3_f32 v1, v1, v74, v75
	v_max3_f32 v1, v1, v76, v77
	v_max3_f32 v1, v1, v78, v79
	v_max3_f32 v1, v1, v80, v81
	v_max3_f32 v1, v1, v82, v83
	v_max3_f32 v1, v1, v84, v85
	v_max3_f32 v1, v1, v86, v87
	v_max3_f32 v1, v1, v88, v89
	v_max3_f32 v1, v1, v90, v91
	v_max3_f32 v1, v1, v92, v93
	v_max3_f32 v1, v1, v94, v95
	v_max3_f32 v1, v1, v96, v97
	v_max3_f32 v1, v1, v98, v99
	v_mov_b32_e32 v2, v1
	s_nop 1
	v_permlane32_swap_b32_e32 v1, v2
	v_max_f32_e32 v2, v2, v2
	v_max_f32_e32 v1, v1, v1
	v_max_f32_e32 v1, v1, v2
	v_cndmask_b32_e64 v1, v168, v1, s[98:99]
	v_sub_f32_e32 v2, v1, v175
	s_mov_b32 s3, 0x42b504f3
	v_cmp_ge_f32_e32 vcc, s3, v2
	s_cmp_eq_u64 vcc, exec
	v_mov_b32_e32 v178, 1.0
	s_cbranch_scc0 .LBB0_1805

.LBB0_1784:
	s_add_i32 s4, s30, -2
	v_lshrrev_b32_e32 v1, s4, v150
	s_sub_i32 s4, s30, 34
	v_lshrrev_b32_e32 v2, s4, v151
	v_cndmask_b32_e64 v1, v2, v1, s[12:13]
	v_and_b32_e32 v1, 1, v1
	v_cmp_ne_u32_e32 vcc, 0, v1
	s_cmp_lg_u64 vcc, 0
	s_cselect_b64 s[16:17], -1, 0
	s_cbranch_vccz .LBB0_1789
	ds_read_b128 v[68:71], v171 offset:49152
	ds_read_b128 v[84:87], v171 offset:57344
	ds_read_b128 v[178:181], v172 offset:49152
	s_cmp_eq_u32 s6, 2
	s_cselect_b64 s[12:13], -1, 0
	v_cndmask_b32_e64 v1, 64, v163, s[12:13]
	s_mov_b64 s[98:99], vcc
	v_cndmask_b32_e32 v1, 0, v1, vcc
	s_cmp_eq_u64 s[12:13], 0
	s_waitcnt lgkmcnt(2)
	v_mfma_f32_32x32x16_bf16 v[68:83], v[68:71], v[100:103], 0
	s_waitcnt lgkmcnt(0)
	v_mfma_f32_32x32x16_bf16 v[68:83], v[178:181], v[108:111], v[68:83]
	ds_read_b128 v[178:181], v172 offset:57344
	v_mfma_f32_32x32x16_bf16 v[84:99], v[84:87], v[100:103], 0
	s_waitcnt lgkmcnt(0)
	v_mfma_f32_32x32x16_bf16 v[84:99], v[178:181], v[108:111], v[84:99]
	ds_read_b128 v[178:181], v173 offset:49152
	s_waitcnt lgkmcnt(0)
	v_mfma_f32_32x32x16_bf16 v[68:83], v[178:181], v[116:119], v[68:83]
	ds_read_b128 v[178:181], v173 offset:57344
	s_waitcnt lgkmcnt(0)
	v_mfma_f32_32x32x16_bf16 v[84:99], v[178:181], v[116:119], v[84:99]
	ds_read_b128 v[178:181], v174 offset:49152
	s_waitcnt lgkmcnt(0)
	v_mfma_f32_32x32x16_bf16 v[68:83], v[178:181], v[124:127], v[68:83]
	ds_read_b128 v[178:181], v174 offset:57344
	s_waitcnt lgkmcnt(0)
	v_mfma_f32_32x32x16_bf16 v[84:99], v[178:181], v[124:127], v[84:99]
	ds_read_b128 v[178:181], v171 offset:49280
	s_waitcnt lgkmcnt(0)
	v_mfma_f32_32x32x16_bf16 v[68:83], v[178:181], v[104:107], v[68:83]
	ds_read_b128 v[178:181], v171 offset:57472
	s_waitcnt lgkmcnt(0)
	v_mfma_f32_32x32x16_bf16 v[84:99], v[178:181], v[104:107], v[84:99]
	ds_read_b128 v[178:181], v172 offset:49280
	s_waitcnt lgkmcnt(0)
	v_mfma_f32_32x32x16_bf16 v[68:83], v[178:181], v[112:115], v[68:83]
	ds_read_b128 v[178:181], v172 offset:57472
	s_waitcnt lgkmcnt(0)
	v_mfma_f32_32x32x16_bf16 v[84:99], v[178:181], v[112:115], v[84:99]
	ds_read_b128 v[178:181], v173 offset:49280
	s_waitcnt lgkmcnt(0)
	v_mfma_f32_32x32x16_bf16 v[68:83], v[178:181], v[120:123], v[68:83]
	ds_read_b128 v[178:181], v173 offset:57472
	s_waitcnt lgkmcnt(0)
	v_mfma_f32_32x32x16_bf16 v[84:99], v[178:181], v[120:123], v[84:99]
	ds_read_b128 v[178:181], v174 offset:49280
	s_waitcnt lgkmcnt(0)
	v_mfma_f32_32x32x16_bf16 v[68:83], v[178:181], v[128:131], v[68:83]
	ds_read_b128 v[178:181], v174 offset:57472
	s_waitcnt lgkmcnt(0)
	v_mfma_f32_32x32x16_bf16 v[84:99], v[178:181], v[128:131], v[84:99]
	s_cbranch_scc1 .LBB0_1787
	v_sub_u32_e32 v1, v1, v137
	v_cmp_lt_i32_e32 vcc, 0, v1
	s_nop 5
	v_cndmask_b32_e32 v68, v168, v68, vcc
	v_cmp_lt_i32_e32 vcc, 32, v1
	s_nop 1
	v_cndmask_b32_e32 v84, v168, v84, vcc
	v_cmp_lt_i32_e32 vcc, 1, v1
	s_nop 1
	v_cndmask_b32_e32 v69, v168, v69, vcc
	v_cmp_lt_i32_e32 vcc, 33, v1
	s_nop 1
	v_cndmask_b32_e32 v85, v168, v85, vcc
	v_cmp_lt_i32_e32 vcc, 2, v1
	s_nop 1
	v_cndmask_b32_e32 v70, v168, v70, vcc
	v_cmp_lt_i32_e32 vcc, 34, v1
	s_nop 1
	v_cndmask_b32_e32 v86, v168, v86, vcc
	v_cmp_lt_i32_e32 vcc, 3, v1
	s_nop 1
	v_cndmask_b32_e32 v71, v168, v71, vcc
	v_cmp_lt_i32_e32 vcc, 35, v1
	s_nop 1
	v_cndmask_b32_e32 v87, v168, v87, vcc
	v_cmp_lt_i32_e32 vcc, 8, v1
	s_nop 1
	v_cndmask_b32_e32 v72, v168, v72, vcc
	v_cmp_lt_i32_e32 vcc, 40, v1
	s_nop 1
	v_cndmask_b32_e32 v88, v168, v88, vcc
	v_cmp_lt_i32_e32 vcc, 9, v1
	s_nop 1
	v_cndmask_b32_e32 v73, v168, v73, vcc
	v_cmp_lt_i32_e32 vcc, 41, v1
	s_nop 1
	v_cndmask_b32_e32 v89, v168, v89, vcc
	v_cmp_lt_i32_e32 vcc, 10, v1
	s_nop 1
	v_cndmask_b32_e32 v74, v168, v74, vcc
	v_cmp_lt_i32_e32 vcc, 42, v1
	s_nop 1
	v_cndmask_b32_e32 v90, v168, v90, vcc
	v_cmp_lt_i32_e32 vcc, 11, v1
	s_nop 1
	v_cndmask_b32_e32 v75, v168, v75, vcc
	v_cmp_lt_i32_e32 vcc, 43, v1
	s_nop 1
	v_cndmask_b32_e32 v91, v168, v91, vcc
	v_cmp_lt_i32_e32 vcc, 16, v1
	s_nop 1
	v_cndmask_b32_e32 v76, v168, v76, vcc
	v_cmp_lt_i32_e32 vcc, 48, v1
	s_nop 1
	v_cndmask_b32_e32 v92, v168, v92, vcc
	v_cmp_lt_i32_e32 vcc, 17, v1
	s_nop 1
	v_cndmask_b32_e32 v77, v168, v77, vcc
	v_cmp_lt_i32_e32 vcc, 49, v1
	s_nop 1
	v_cndmask_b32_e32 v93, v168, v93, vcc
	v_cmp_lt_i32_e32 vcc, 18, v1
	s_nop 1
	v_cndmask_b32_e32 v78, v168, v78, vcc
	v_cmp_lt_i32_e32 vcc, 50, v1
	s_nop 1
	v_cndmask_b32_e32 v94, v168, v94, vcc
	v_cmp_lt_i32_e32 vcc, 19, v1
	s_nop 1
	v_cndmask_b32_e32 v79, v168, v79, vcc
	v_cmp_lt_i32_e32 vcc, 51, v1
	s_nop 1
	v_cndmask_b32_e32 v95, v168, v95, vcc
	v_cmp_lt_i32_e32 vcc, 24, v1
	s_nop 1
	v_cndmask_b32_e32 v80, v168, v80, vcc
	v_cmp_lt_i32_e32 vcc, 56, v1
	s_nop 1
	v_cndmask_b32_e32 v96, v168, v96, vcc
	v_cmp_lt_i32_e32 vcc, 25, v1
	s_nop 1
	v_cndmask_b32_e32 v81, v168, v81, vcc
	v_cmp_lt_i32_e32 vcc, 57, v1
	s_nop 1
	v_cndmask_b32_e32 v97, v168, v97, vcc
	v_cmp_lt_i32_e32 vcc, 26, v1
	s_nop 1
	v_cndmask_b32_e32 v82, v168, v82, vcc
	v_cmp_lt_i32_e32 vcc, 58, v1
	s_nop 1
	v_cndmask_b32_e32 v98, v168, v98, vcc
	v_cmp_lt_i32_e32 vcc, 27, v1
	s_nop 1
	v_cndmask_b32_e32 v83, v168, v83, vcc
	v_cmp_lt_i32_e32 vcc, 59, v1
	s_nop 1
	v_cndmask_b32_e32 v99, v168, v99, vcc
.LBB0_1787:
	s_nop 7
	v_max_f32_e32 v1, v69, v69
	v_max_f32_e32 v2, v68, v68
	v_max_f32_e32 v1, v2, v1
	v_max3_f32 v1, v1, v70, v71
	v_max3_f32 v1, v1, v72, v73
	v_max3_f32 v1, v1, v74, v75
	v_max3_f32 v1, v1, v76, v77
	v_max3_f32 v1, v1, v78, v79
	v_max3_f32 v1, v1, v80, v81
	v_max3_f32 v1, v1, v82, v83
	v_max3_f32 v1, v1, v84, v85
	v_max3_f32 v1, v1, v86, v87
	v_max3_f32 v1, v1, v88, v89
	v_max3_f32 v1, v1, v90, v91
	v_max3_f32 v1, v1, v92, v93
	v_max3_f32 v1, v1, v94, v95
	v_max3_f32 v1, v1, v96, v97
	v_max3_f32 v1, v1, v98, v99
	v_mov_b32_e32 v2, v1
	s_nop 1
	v_permlane32_swap_b32_e32 v1, v2
	v_max_f32_e32 v2, v2, v2
	v_max_f32_e32 v1, v1, v1
	v_max_f32_e32 v1, v1, v2
	v_cndmask_b32_e64 v1, v168, v1, s[98:99]
	v_sub_f32_e32 v2, v1, v175
	s_mov_b32 s4, 0x42b504f3
	v_cmp_ge_f32_e32 vcc, s4, v2
	s_cmp_eq_u64 vcc, exec
	v_mov_b32_e32 v178, 1.0
	s_cbranch_scc0 .LBB0_1806

.LBB0_1827:
	v_bfe_u32 v1, v150, 1, 1
	v_cmp_ne_u32_e32 vcc, 0, v1
	s_cmp_lg_u64 vcc, 0
	s_cselect_b64 s[12:13], -1, 0
	s_cbranch_vccz .LBB0_1832
	ds_read_b128 v[68:71], v142 offset:49152
	ds_read_b128 v[84:87], v142 offset:57344
	ds_read_b128 v[170:173], v143 offset:49152
	v_cndmask_b32_e64 v1, 64, v163, s[10:11]
	s_mov_b64 s[98:99], vcc
	v_cndmask_b32_e32 v1, 0, v1, vcc
	s_cmp_eq_u64 s[10:11], 0
	s_waitcnt lgkmcnt(2)
	v_mfma_f32_32x32x16_bf16 v[68:83], v[68:71], v[100:103], 0
	s_waitcnt lgkmcnt(0)
	v_mfma_f32_32x32x16_bf16 v[68:83], v[170:173], v[108:111], v[68:83]
	ds_read_b128 v[170:173], v143 offset:57344
	v_mfma_f32_32x32x16_bf16 v[84:99], v[84:87], v[100:103], 0
	s_waitcnt lgkmcnt(0)
	v_mfma_f32_32x32x16_bf16 v[84:99], v[170:173], v[108:111], v[84:99]
	ds_read_b128 v[170:173], v152 offset:49152
	s_waitcnt lgkmcnt(0)
	v_mfma_f32_32x32x16_bf16 v[68:83], v[170:173], v[116:119], v[68:83]
	ds_read_b128 v[170:173], v152 offset:57344
	s_waitcnt lgkmcnt(0)
	v_mfma_f32_32x32x16_bf16 v[84:99], v[170:173], v[116:119], v[84:99]
	ds_read_b128 v[170:173], v153 offset:49152
	s_waitcnt lgkmcnt(0)
	v_mfma_f32_32x32x16_bf16 v[68:83], v[170:173], v[124:127], v[68:83]
	ds_read_b128 v[170:173], v153 offset:57344
	s_waitcnt lgkmcnt(0)
	v_mfma_f32_32x32x16_bf16 v[84:99], v[170:173], v[124:127], v[84:99]
	ds_read_b128 v[170:173], v142 offset:49280
	s_waitcnt lgkmcnt(0)
	v_mfma_f32_32x32x16_bf16 v[68:83], v[170:173], v[104:107], v[68:83]
	ds_read_b128 v[170:173], v142 offset:57472
	s_waitcnt lgkmcnt(0)
	v_mfma_f32_32x32x16_bf16 v[84:99], v[170:173], v[104:107], v[84:99]
	ds_read_b128 v[170:173], v143 offset:49280
	s_waitcnt lgkmcnt(0)
	v_mfma_f32_32x32x16_bf16 v[68:83], v[170:173], v[112:115], v[68:83]
	ds_read_b128 v[170:173], v143 offset:57472
	s_waitcnt lgkmcnt(0)
	v_mfma_f32_32x32x16_bf16 v[84:99], v[170:173], v[112:115], v[84:99]
	ds_read_b128 v[170:173], v152 offset:49280
	s_waitcnt lgkmcnt(0)
	v_mfma_f32_32x32x16_bf16 v[68:83], v[170:173], v[120:123], v[68:83]
	ds_read_b128 v[170:173], v152 offset:57472
	s_waitcnt lgkmcnt(0)
	v_mfma_f32_32x32x16_bf16 v[84:99], v[170:173], v[120:123], v[84:99]
	ds_read_b128 v[170:173], v153 offset:49280
	s_waitcnt lgkmcnt(0)
	v_mfma_f32_32x32x16_bf16 v[68:83], v[170:173], v[128:131], v[68:83]
	ds_read_b128 v[170:173], v153 offset:57472
	s_waitcnt lgkmcnt(0)
	v_mfma_f32_32x32x16_bf16 v[84:99], v[170:173], v[128:131], v[84:99]
	s_cbranch_scc1 .LBB0_1830
	v_sub_u32_e32 v1, v1, v137
	v_cmp_lt_i32_e32 vcc, 0, v1
	s_nop 5
	v_cndmask_b32_e32 v68, v168, v68, vcc
	v_cmp_lt_i32_e32 vcc, 32, v1
	s_nop 1
	v_cndmask_b32_e32 v84, v168, v84, vcc
	v_cmp_lt_i32_e32 vcc, 1, v1
	s_nop 1
	v_cndmask_b32_e32 v69, v168, v69, vcc
	v_cmp_lt_i32_e32 vcc, 33, v1
	s_nop 1
	v_cndmask_b32_e32 v85, v168, v85, vcc
	v_cmp_lt_i32_e32 vcc, 2, v1
	s_nop 1
	v_cndmask_b32_e32 v70, v168, v70, vcc
	v_cmp_lt_i32_e32 vcc, 34, v1
	s_nop 1
	v_cndmask_b32_e32 v86, v168, v86, vcc
	v_cmp_lt_i32_e32 vcc, 3, v1
	s_nop 1
	v_cndmask_b32_e32 v71, v168, v71, vcc
	v_cmp_lt_i32_e32 vcc, 35, v1
	s_nop 1
	v_cndmask_b32_e32 v87, v168, v87, vcc
	v_cmp_lt_i32_e32 vcc, 8, v1
	s_nop 1
	v_cndmask_b32_e32 v72, v168, v72, vcc
	v_cmp_lt_i32_e32 vcc, 40, v1
	s_nop 1
	v_cndmask_b32_e32 v88, v168, v88, vcc
	v_cmp_lt_i32_e32 vcc, 9, v1
	s_nop 1
	v_cndmask_b32_e32 v73, v168, v73, vcc
	v_cmp_lt_i32_e32 vcc, 41, v1
	s_nop 1
	v_cndmask_b32_e32 v89, v168, v89, vcc
	v_cmp_lt_i32_e32 vcc, 10, v1
	s_nop 1
	v_cndmask_b32_e32 v74, v168, v74, vcc
	v_cmp_lt_i32_e32 vcc, 42, v1
	s_nop 1
	v_cndmask_b32_e32 v90, v168, v90, vcc
	v_cmp_lt_i32_e32 vcc, 11, v1
	s_nop 1
	v_cndmask_b32_e32 v75, v168, v75, vcc
	v_cmp_lt_i32_e32 vcc, 43, v1
	s_nop 1
	v_cndmask_b32_e32 v91, v168, v91, vcc
	v_cmp_lt_i32_e32 vcc, 16, v1
	s_nop 1
	v_cndmask_b32_e32 v76, v168, v76, vcc
	v_cmp_lt_i32_e32 vcc, 48, v1
	s_nop 1
	v_cndmask_b32_e32 v92, v168, v92, vcc
	v_cmp_lt_i32_e32 vcc, 17, v1
	s_nop 1
	v_cndmask_b32_e32 v77, v168, v77, vcc
	v_cmp_lt_i32_e32 vcc, 49, v1
	s_nop 1
	v_cndmask_b32_e32 v93, v168, v93, vcc
	v_cmp_lt_i32_e32 vcc, 18, v1
	s_nop 1
	v_cndmask_b32_e32 v78, v168, v78, vcc
	v_cmp_lt_i32_e32 vcc, 50, v1
	s_nop 1
	v_cndmask_b32_e32 v94, v168, v94, vcc
	v_cmp_lt_i32_e32 vcc, 19, v1
	s_nop 1
	v_cndmask_b32_e32 v79, v168, v79, vcc
	v_cmp_lt_i32_e32 vcc, 51, v1
	s_nop 1
	v_cndmask_b32_e32 v95, v168, v95, vcc
	v_cmp_lt_i32_e32 vcc, 24, v1
	s_nop 1
	v_cndmask_b32_e32 v80, v168, v80, vcc
	v_cmp_lt_i32_e32 vcc, 56, v1
	s_nop 1
	v_cndmask_b32_e32 v96, v168, v96, vcc
	v_cmp_lt_i32_e32 vcc, 25, v1
	s_nop 1
	v_cndmask_b32_e32 v81, v168, v81, vcc
	v_cmp_lt_i32_e32 vcc, 57, v1
	s_nop 1
	v_cndmask_b32_e32 v97, v168, v97, vcc
	v_cmp_lt_i32_e32 vcc, 26, v1
	s_nop 1
	v_cndmask_b32_e32 v82, v168, v82, vcc
	v_cmp_lt_i32_e32 vcc, 58, v1
	s_nop 1
	v_cndmask_b32_e32 v98, v168, v98, vcc
	v_cmp_lt_i32_e32 vcc, 27, v1
	s_nop 1
	v_cndmask_b32_e32 v83, v168, v83, vcc
	v_cmp_lt_i32_e32 vcc, 59, v1
	s_nop 1
	v_cndmask_b32_e32 v99, v168, v99, vcc
.LBB0_1830:
	s_nop 7
	v_max_f32_e32 v1, v69, v69
	v_max_f32_e32 v2, v68, v68
	v_max_f32_e32 v1, v2, v1
	v_max3_f32 v1, v1, v70, v71
	v_max3_f32 v1, v1, v72, v73
	v_max3_f32 v1, v1, v74, v75
	v_max3_f32 v1, v1, v76, v77
	v_max3_f32 v1, v1, v78, v79
	v_max3_f32 v1, v1, v80, v81
	v_max3_f32 v1, v1, v82, v83
	v_max3_f32 v1, v1, v84, v85
	v_max3_f32 v1, v1, v86, v87
	v_max3_f32 v1, v1, v88, v89
	v_max3_f32 v1, v1, v90, v91
	v_max3_f32 v1, v1, v92, v93
	v_max3_f32 v1, v1, v94, v95
	v_max3_f32 v1, v1, v96, v97
	v_max3_f32 v1, v1, v98, v99
	v_mov_b32_e32 v2, v1
	s_nop 1
	v_permlane32_swap_b32_e32 v1, v2
	v_max_f32_e32 v2, v2, v2
	v_max_f32_e32 v1, v1, v1
	v_max_f32_e32 v1, v1, v2
	v_cndmask_b32_e64 v1, v168, v1, s[98:99]
	v_sub_f32_e32 v2, v1, v154
	s_mov_b32 s1, 0x42b504f3
	v_cmp_ge_f32_e32 vcc, s1, v2
	s_cmp_eq_u64 vcc, exec
	v_mov_b32_e32 v155, 1.0
	s_cbranch_scc0 .LBB0_2103
.LBB0_1831:
	v_mul_f32_e32 v2, 0xbe0293ee, v154
	v_cndmask_b32_e64 v2, v168, v2, s[98:99]
	v_pk_fma_f32 v[68:69], v[68:69], s[2:3], v[2:3] op_sel_hi:[1,0,0]
	v_pk_fma_f32 v[70:71], v[70:71], s[2:3], v[2:3] op_sel_hi:[1,0,0]
	v_pk_fma_f32 v[72:73], v[72:73], s[2:3], v[2:3] op_sel_hi:[1,0,0]
	v_pk_fma_f32 v[74:75], v[74:75], s[2:3], v[2:3] op_sel_hi:[1,0,0]
	v_pk_fma_f32 v[76:77], v[76:77], s[2:3], v[2:3] op_sel_hi:[1,0,0]
	v_pk_fma_f32 v[78:79], v[78:79], s[2:3], v[2:3] op_sel_hi:[1,0,0]
	v_pk_fma_f32 v[80:81], v[80:81], s[2:3], v[2:3] op_sel_hi:[1,0,0]
	v_pk_fma_f32 v[82:83], v[82:83], s[2:3], v[2:3] op_sel_hi:[1,0,0]
	v_exp_f32_e32 v68, v68
	v_exp_f32_e32 v69, v69
	v_exp_f32_e32 v70, v70
	v_exp_f32_e32 v71, v71
	v_exp_f32_e32 v72, v72
	v_exp_f32_e32 v73, v73
	v_exp_f32_e32 v74, v74
	v_exp_f32_e32 v75, v75
	v_exp_f32_e32 v76, v76
	v_exp_f32_e32 v77, v77
	v_exp_f32_e32 v78, v78
	v_exp_f32_e32 v79, v79
	v_exp_f32_e32 v80, v80
	v_exp_f32_e32 v81, v81
	v_exp_f32_e32 v82, v82
	v_exp_f32_e32 v83, v83
	v_pk_fma_f32 v[86:87], v[86:87], s[2:3], v[2:3] op_sel_hi:[1,0,0]
	v_pk_fma_f32 v[84:85], v[84:85], s[2:3], v[2:3] op_sel_hi:[1,0,0]
	v_pk_fma_f32 v[88:89], v[88:89], s[2:3], v[2:3] op_sel_hi:[1,0,0]
	v_pk_fma_f32 v[90:91], v[90:91], s[2:3], v[2:3] op_sel_hi:[1,0,0]
	v_pk_fma_f32 v[92:93], v[92:93], s[2:3], v[2:3] op_sel_hi:[1,0,0]
	v_pk_fma_f32 v[94:95], v[94:95], s[2:3], v[2:3] op_sel_hi:[1,0,0]
	v_pk_fma_f32 v[96:97], v[96:97], s[2:3], v[2:3] op_sel_hi:[1,0,0]
	v_pk_fma_f32 v[98:99], v[98:99], s[2:3], v[2:3] op_sel_hi:[1,0,0]

.LBB0_1853:
	s_add_i32 s3, s1, s28
	s_cmp_lt_u32 s4, 32
	v_lshrrev_b32_e32 v1, s4, v150
	s_cselect_b64 s[10:11], -1, 0
	s_sub_i32 s4, s28, 34
	v_lshrrev_b32_e32 v2, s4, v151
	v_cndmask_b32_e64 v1, v2, v1, s[10:11]
	v_and_b32_e32 v1, 1, v1
	v_cmp_ne_u32_e32 vcc, 0, v1
	s_cmp_lg_u64 vcc, 0
	s_cselect_b64 s[18:19], -1, 0
	s_cbranch_vccz .LBB0_1858
	ds_read_b128 v[68:71], v142 offset:32768
	ds_read_b128 v[84:87], v142 offset:40960
	ds_read_b128 v[170:173], v143 offset:32768
	s_cmp_eq_u32 s3, 2
	s_cselect_b64 s[12:13], -1, 0
	v_cndmask_b32_e64 v1, 64, v163, s[12:13]
	s_mov_b64 s[98:99], vcc
	v_cndmask_b32_e32 v1, 0, v1, vcc
	s_cmp_eq_u64 s[12:13], 0
	s_waitcnt lgkmcnt(2)
	v_mfma_f32_32x32x16_bf16 v[68:83], v[68:71], v[100:103], 0
	s_waitcnt lgkmcnt(0)
	v_mfma_f32_32x32x16_bf16 v[68:83], v[170:173], v[108:111], v[68:83]
	ds_read_b128 v[170:173], v143 offset:40960
	v_mfma_f32_32x32x16_bf16 v[84:99], v[84:87], v[100:103], 0
	s_waitcnt lgkmcnt(0)
	v_mfma_f32_32x32x16_bf16 v[84:99], v[170:173], v[108:111], v[84:99]
	ds_read_b128 v[170:173], v152 offset:32768
	s_waitcnt lgkmcnt(0)
	v_mfma_f32_32x32x16_bf16 v[68:83], v[170:173], v[116:119], v[68:83]
	ds_read_b128 v[170:173], v152 offset:40960
	s_waitcnt lgkmcnt(0)
	v_mfma_f32_32x32x16_bf16 v[84:99], v[170:173], v[116:119], v[84:99]
	ds_read_b128 v[170:173], v153 offset:32768
	s_waitcnt lgkmcnt(0)
	v_mfma_f32_32x32x16_bf16 v[68:83], v[170:173], v[124:127], v[68:83]
	ds_read_b128 v[170:173], v153 offset:40960
	s_waitcnt lgkmcnt(0)
	v_mfma_f32_32x32x16_bf16 v[84:99], v[170:173], v[124:127], v[84:99]
	ds_read_b128 v[170:173], v142 offset:32896
	s_waitcnt lgkmcnt(0)
	v_mfma_f32_32x32x16_bf16 v[68:83], v[170:173], v[104:107], v[68:83]
	ds_read_b128 v[170:173], v142 offset:41088
	s_waitcnt lgkmcnt(0)
	v_mfma_f32_32x32x16_bf16 v[84:99], v[170:173], v[104:107], v[84:99]
	ds_read_b128 v[170:173], v143 offset:32896
	s_waitcnt lgkmcnt(0)
	v_mfma_f32_32x32x16_bf16 v[68:83], v[170:173], v[112:115], v[68:83]
	ds_read_b128 v[170:173], v143 offset:41088
	s_waitcnt lgkmcnt(0)
	v_mfma_f32_32x32x16_bf16 v[84:99], v[170:173], v[112:115], v[84:99]
	ds_read_b128 v[170:173], v152 offset:32896
	s_waitcnt lgkmcnt(0)
	v_mfma_f32_32x32x16_bf16 v[68:83], v[170:173], v[120:123], v[68:83]
	ds_read_b128 v[170:173], v152 offset:41088
	s_waitcnt lgkmcnt(0)
	v_mfma_f32_32x32x16_bf16 v[84:99], v[170:173], v[120:123], v[84:99]
	ds_read_b128 v[170:173], v153 offset:32896
	s_waitcnt lgkmcnt(0)
	v_mfma_f32_32x32x16_bf16 v[68:83], v[170:173], v[128:131], v[68:83]
	ds_read_b128 v[170:173], v153 offset:41088
	s_waitcnt lgkmcnt(0)
	v_mfma_f32_32x32x16_bf16 v[84:99], v[170:173], v[128:131], v[84:99]
	s_cbranch_scc1 .LBB0_1856
	v_sub_u32_e32 v1, v1, v137
	v_cmp_lt_i32_e32 vcc, 0, v1
	s_nop 5
	v_cndmask_b32_e32 v68, v168, v68, vcc
	v_cmp_lt_i32_e32 vcc, 32, v1
	s_nop 1
	v_cndmask_b32_e32 v84, v168, v84, vcc
	v_cmp_lt_i32_e32 vcc, 1, v1
	s_nop 1
	v_cndmask_b32_e32 v69, v168, v69, vcc
	v_cmp_lt_i32_e32 vcc, 33, v1
	s_nop 1
	v_cndmask_b32_e32 v85, v168, v85, vcc
	v_cmp_lt_i32_e32 vcc, 2, v1
	s_nop 1
	v_cndmask_b32_e32 v70, v168, v70, vcc
	v_cmp_lt_i32_e32 vcc, 34, v1
	s_nop 1
	v_cndmask_b32_e32 v86, v168, v86, vcc
	v_cmp_lt_i32_e32 vcc, 3, v1
	s_nop 1
	v_cndmask_b32_e32 v71, v168, v71, vcc
	v_cmp_lt_i32_e32 vcc, 35, v1
	s_nop 1
	v_cndmask_b32_e32 v87, v168, v87, vcc
	v_cmp_lt_i32_e32 vcc, 8, v1
	s_nop 1
	v_cndmask_b32_e32 v72, v168, v72, vcc
	v_cmp_lt_i32_e32 vcc, 40, v1
	s_nop 1
	v_cndmask_b32_e32 v88, v168, v88, vcc
	v_cmp_lt_i32_e32 vcc, 9, v1
	s_nop 1
	v_cndmask_b32_e32 v73, v168, v73, vcc
	v_cmp_lt_i32_e32 vcc, 41, v1
	s_nop 1
	v_cndmask_b32_e32 v89, v168, v89, vcc
	v_cmp_lt_i32_e32 vcc, 10, v1
	s_nop 1
	v_cndmask_b32_e32 v74, v168, v74, vcc
	v_cmp_lt_i32_e32 vcc, 42, v1
	s_nop 1
	v_cndmask_b32_e32 v90, v168, v90, vcc
	v_cmp_lt_i32_e32 vcc, 11, v1
	s_nop 1
	v_cndmask_b32_e32 v75, v168, v75, vcc
	v_cmp_lt_i32_e32 vcc, 43, v1
	s_nop 1
	v_cndmask_b32_e32 v91, v168, v91, vcc
	v_cmp_lt_i32_e32 vcc, 16, v1
	s_nop 1
	v_cndmask_b32_e32 v76, v168, v76, vcc
	v_cmp_lt_i32_e32 vcc, 48, v1
	s_nop 1
	v_cndmask_b32_e32 v92, v168, v92, vcc
	v_cmp_lt_i32_e32 vcc, 17, v1
	s_nop 1
	v_cndmask_b32_e32 v77, v168, v77, vcc
	v_cmp_lt_i32_e32 vcc, 49, v1
	s_nop 1
	v_cndmask_b32_e32 v93, v168, v93, vcc
	v_cmp_lt_i32_e32 vcc, 18, v1
	s_nop 1
	v_cndmask_b32_e32 v78, v168, v78, vcc
	v_cmp_lt_i32_e32 vcc, 50, v1
	s_nop 1
	v_cndmask_b32_e32 v94, v168, v94, vcc
	v_cmp_lt_i32_e32 vcc, 19, v1
	s_nop 1
	v_cndmask_b32_e32 v79, v168, v79, vcc
	v_cmp_lt_i32_e32 vcc, 51, v1
	s_nop 1
	v_cndmask_b32_e32 v95, v168, v95, vcc
	v_cmp_lt_i32_e32 vcc, 24, v1
	s_nop 1
	v_cndmask_b32_e32 v80, v168, v80, vcc
	v_cmp_lt_i32_e32 vcc, 56, v1
	s_nop 1
	v_cndmask_b32_e32 v96, v168, v96, vcc
	v_cmp_lt_i32_e32 vcc, 25, v1
	s_nop 1
	v_cndmask_b32_e32 v81, v168, v81, vcc
	v_cmp_lt_i32_e32 vcc, 57, v1
	s_nop 1
	v_cndmask_b32_e32 v97, v168, v97, vcc
	v_cmp_lt_i32_e32 vcc, 26, v1
	s_nop 1
	v_cndmask_b32_e32 v82, v168, v82, vcc
	v_cmp_lt_i32_e32 vcc, 58, v1
	s_nop 1
	v_cndmask_b32_e32 v98, v168, v98, vcc
	v_cmp_lt_i32_e32 vcc, 27, v1
	s_nop 1
	v_cndmask_b32_e32 v83, v168, v83, vcc
	v_cmp_lt_i32_e32 vcc, 59, v1
	s_nop 1
	v_cndmask_b32_e32 v99, v168, v99, vcc
.LBB0_1856:
	s_nop 7
	v_max_f32_e32 v1, v69, v69
	v_max_f32_e32 v2, v68, v68
	v_max_f32_e32 v1, v2, v1
	v_max3_f32 v1, v1, v70, v71
	v_max3_f32 v1, v1, v72, v73
	v_max3_f32 v1, v1, v74, v75
	v_max3_f32 v1, v1, v76, v77
	v_max3_f32 v1, v1, v78, v79
	v_max3_f32 v1, v1, v80, v81
	v_max3_f32 v1, v1, v82, v83
	v_max3_f32 v1, v1, v84, v85
	v_max3_f32 v1, v1, v86, v87
	v_max3_f32 v1, v1, v88, v89
	v_max3_f32 v1, v1, v90, v91
	v_max3_f32 v1, v1, v92, v93
	v_max3_f32 v1, v1, v94, v95
	v_max3_f32 v1, v1, v96, v97
	v_max3_f32 v1, v1, v98, v99
	v_mov_b32_e32 v2, v1
	s_nop 1
	v_permlane32_swap_b32_e32 v1, v2
	v_max_f32_e32 v2, v2, v2
	v_max_f32_e32 v1, v1, v1
	v_max_f32_e32 v1, v1, v2
	v_cndmask_b32_e64 v1, v168, v1, s[98:99]
	v_sub_f32_e32 v2, v1, v154
	s_mov_b32 s4, 0x42b504f3
	v_cmp_ge_f32_e32 vcc, s4, v2
	s_cmp_eq_u64 vcc, exec
	v_mov_b32_e32 v155, 1.0
	s_cbranch_scc0 .LBB0_1901

.LBB0_1877:
	s_add_i32 s4, s28, -1
	v_lshrrev_b32_e32 v1, s4, v150
	s_sub_i32 s4, s28, 33
	v_lshrrev_b32_e32 v2, s4, v151
	v_cndmask_b32_e64 v1, v2, v1, s[10:11]
	v_and_b32_e32 v1, 1, v1
	v_cmp_ne_u32_e32 vcc, 0, v1
	s_cmp_lg_u64 vcc, 0
	s_cselect_b64 s[12:13], -1, 0
	s_cbranch_vccz .LBB0_1882
	ds_read_b128 v[68:71], v142 offset:49152
	ds_read_b128 v[84:87], v142 offset:57344
	ds_read_b128 v[170:173], v143 offset:49152
	s_cmp_eq_u32 s3, 1
	s_cselect_b64 s[10:11], -1, 0
	v_cndmask_b32_e64 v1, 64, v163, s[10:11]
	s_mov_b64 s[98:99], vcc
	v_cndmask_b32_e32 v1, 0, v1, vcc
	s_cmp_eq_u64 s[10:11], 0
	s_waitcnt lgkmcnt(2)
	v_mfma_f32_32x32x16_bf16 v[68:83], v[68:71], v[100:103], 0
	s_waitcnt lgkmcnt(0)
	v_mfma_f32_32x32x16_bf16 v[68:83], v[170:173], v[108:111], v[68:83]
	ds_read_b128 v[170:173], v143 offset:57344
	v_mfma_f32_32x32x16_bf16 v[84:99], v[84:87], v[100:103], 0
	s_waitcnt lgkmcnt(0)
	v_mfma_f32_32x32x16_bf16 v[84:99], v[170:173], v[108:111], v[84:99]
	ds_read_b128 v[170:173], v152 offset:49152
	s_waitcnt lgkmcnt(0)
	v_mfma_f32_32x32x16_bf16 v[68:83], v[170:173], v[116:119], v[68:83]
	ds_read_b128 v[170:173], v152 offset:57344
	s_waitcnt lgkmcnt(0)
	v_mfma_f32_32x32x16_bf16 v[84:99], v[170:173], v[116:119], v[84:99]
	ds_read_b128 v[170:173], v153 offset:49152
	s_waitcnt lgkmcnt(0)
	v_mfma_f32_32x32x16_bf16 v[68:83], v[170:173], v[124:127], v[68:83]
	ds_read_b128 v[170:173], v153 offset:57344
	s_waitcnt lgkmcnt(0)
	v_mfma_f32_32x32x16_bf16 v[84:99], v[170:173], v[124:127], v[84:99]
	ds_read_b128 v[170:173], v142 offset:49280
	s_waitcnt lgkmcnt(0)
	v_mfma_f32_32x32x16_bf16 v[68:83], v[170:173], v[104:107], v[68:83]
	ds_read_b128 v[170:173], v142 offset:57472
	s_waitcnt lgkmcnt(0)
	v_mfma_f32_32x32x16_bf16 v[84:99], v[170:173], v[104:107], v[84:99]
	ds_read_b128 v[170:173], v143 offset:49280
	s_waitcnt lgkmcnt(0)
	v_mfma_f32_32x32x16_bf16 v[68:83], v[170:173], v[112:115], v[68:83]
	ds_read_b128 v[170:173], v143 offset:57472
	s_waitcnt lgkmcnt(0)
	v_mfma_f32_32x32x16_bf16 v[84:99], v[170:173], v[112:115], v[84:99]
	ds_read_b128 v[170:173], v152 offset:49280
	s_waitcnt lgkmcnt(0)
	v_mfma_f32_32x32x16_bf16 v[68:83], v[170:173], v[120:123], v[68:83]
	ds_read_b128 v[170:173], v152 offset:57472
	s_waitcnt lgkmcnt(0)
	v_mfma_f32_32x32x16_bf16 v[84:99], v[170:173], v[120:123], v[84:99]
	ds_read_b128 v[170:173], v153 offset:49280
	s_waitcnt lgkmcnt(0)
	v_mfma_f32_32x32x16_bf16 v[68:83], v[170:173], v[128:131], v[68:83]
	ds_read_b128 v[170:173], v153 offset:57472
	s_waitcnt lgkmcnt(0)
	v_mfma_f32_32x32x16_bf16 v[84:99], v[170:173], v[128:131], v[84:99]
	s_cbranch_scc1 .LBB0_1880
	v_sub_u32_e32 v1, v1, v137
	v_cmp_lt_i32_e32 vcc, 0, v1
	s_nop 5
	v_cndmask_b32_e32 v68, v168, v68, vcc
	v_cmp_lt_i32_e32 vcc, 32, v1
	s_nop 1
	v_cndmask_b32_e32 v84, v168, v84, vcc
	v_cmp_lt_i32_e32 vcc, 1, v1
	s_nop 1
	v_cndmask_b32_e32 v69, v168, v69, vcc
	v_cmp_lt_i32_e32 vcc, 33, v1
	s_nop 1
	v_cndmask_b32_e32 v85, v168, v85, vcc
	v_cmp_lt_i32_e32 vcc, 2, v1
	s_nop 1
	v_cndmask_b32_e32 v70, v168, v70, vcc
	v_cmp_lt_i32_e32 vcc, 34, v1
	s_nop 1
	v_cndmask_b32_e32 v86, v168, v86, vcc
	v_cmp_lt_i32_e32 vcc, 3, v1
	s_nop 1
	v_cndmask_b32_e32 v71, v168, v71, vcc
	v_cmp_lt_i32_e32 vcc, 35, v1
	s_nop 1
	v_cndmask_b32_e32 v87, v168, v87, vcc
	v_cmp_lt_i32_e32 vcc, 8, v1
	s_nop 1
	v_cndmask_b32_e32 v72, v168, v72, vcc
	v_cmp_lt_i32_e32 vcc, 40, v1
	s_nop 1
	v_cndmask_b32_e32 v88, v168, v88, vcc
	v_cmp_lt_i32_e32 vcc, 9, v1
	s_nop 1
	v_cndmask_b32_e32 v73, v168, v73, vcc
	v_cmp_lt_i32_e32 vcc, 41, v1
	s_nop 1
	v_cndmask_b32_e32 v89, v168, v89, vcc
	v_cmp_lt_i32_e32 vcc, 10, v1
	s_nop 1
	v_cndmask_b32_e32 v74, v168, v74, vcc
	v_cmp_lt_i32_e32 vcc, 42, v1
	s_nop 1
	v_cndmask_b32_e32 v90, v168, v90, vcc
	v_cmp_lt_i32_e32 vcc, 11, v1
	s_nop 1
	v_cndmask_b32_e32 v75, v168, v75, vcc
	v_cmp_lt_i32_e32 vcc, 43, v1
	s_nop 1
	v_cndmask_b32_e32 v91, v168, v91, vcc
	v_cmp_lt_i32_e32 vcc, 16, v1
	s_nop 1
	v_cndmask_b32_e32 v76, v168, v76, vcc
	v_cmp_lt_i32_e32 vcc, 48, v1
	s_nop 1
	v_cndmask_b32_e32 v92, v168, v92, vcc
	v_cmp_lt_i32_e32 vcc, 17, v1
	s_nop 1
	v_cndmask_b32_e32 v77, v168, v77, vcc
	v_cmp_lt_i32_e32 vcc, 49, v1
	s_nop 1
	v_cndmask_b32_e32 v93, v168, v93, vcc
	v_cmp_lt_i32_e32 vcc, 18, v1
	s_nop 1
	v_cndmask_b32_e32 v78, v168, v78, vcc
	v_cmp_lt_i32_e32 vcc, 50, v1
	s_nop 1
	v_cndmask_b32_e32 v94, v168, v94, vcc
	v_cmp_lt_i32_e32 vcc, 19, v1
	s_nop 1
	v_cndmask_b32_e32 v79, v168, v79, vcc
	v_cmp_lt_i32_e32 vcc, 51, v1
	s_nop 1
	v_cndmask_b32_e32 v95, v168, v95, vcc
	v_cmp_lt_i32_e32 vcc, 24, v1
	s_nop 1
	v_cndmask_b32_e32 v80, v168, v80, vcc
	v_cmp_lt_i32_e32 vcc, 56, v1
	s_nop 1
	v_cndmask_b32_e32 v96, v168, v96, vcc
	v_cmp_lt_i32_e32 vcc, 25, v1
	s_nop 1
	v_cndmask_b32_e32 v81, v168, v81, vcc
	v_cmp_lt_i32_e32 vcc, 57, v1
	s_nop 1
	v_cndmask_b32_e32 v97, v168, v97, vcc
	v_cmp_lt_i32_e32 vcc, 26, v1
	s_nop 1
	v_cndmask_b32_e32 v82, v168, v82, vcc
	v_cmp_lt_i32_e32 vcc, 58, v1
	s_nop 1
	v_cndmask_b32_e32 v98, v168, v98, vcc
	v_cmp_lt_i32_e32 vcc, 27, v1
	s_nop 1
	v_cndmask_b32_e32 v83, v168, v83, vcc
	v_cmp_lt_i32_e32 vcc, 59, v1
	s_nop 1
	v_cndmask_b32_e32 v99, v168, v99, vcc
.LBB0_1880:
	s_nop 7
	v_max_f32_e32 v1, v69, v69
	v_max_f32_e32 v2, v68, v68
	v_max_f32_e32 v1, v2, v1
	v_max3_f32 v1, v1, v70, v71
	v_max3_f32 v1, v1, v72, v73
	v_max3_f32 v1, v1, v74, v75
	v_max3_f32 v1, v1, v76, v77
	v_max3_f32 v1, v1, v78, v79
	v_max3_f32 v1, v1, v80, v81
	v_max3_f32 v1, v1, v82, v83
	v_max3_f32 v1, v1, v84, v85
	v_max3_f32 v1, v1, v86, v87
	v_max3_f32 v1, v1, v88, v89
	v_max3_f32 v1, v1, v90, v91
	v_max3_f32 v1, v1, v92, v93
	v_max3_f32 v1, v1, v94, v95
	v_max3_f32 v1, v1, v96, v97
	v_max3_f32 v1, v1, v98, v99
	v_mov_b32_e32 v2, v1
	s_nop 1
	v_permlane32_swap_b32_e32 v1, v2
	v_max_f32_e32 v2, v2, v2
	v_max_f32_e32 v1, v1, v1
	v_max_f32_e32 v1, v1, v2
	v_cndmask_b32_e64 v1, v168, v1, s[98:99]
	v_sub_f32_e32 v2, v1, v154
	s_mov_b32 s3, 0x42b504f3
	v_cmp_ge_f32_e32 vcc, s3, v2
	s_cmp_eq_u64 vcc, exec
	v_mov_b32_e32 v155, 1.0
	s_cbranch_scc0 .LBB0_1902

	.amdhsa_kernel _Z8mega_fwd4Args
		.amdhsa_group_segment_fixed_size 0
		.amdhsa_private_segment_fixed_size 0
		.amdhsa_kernarg_size 520
		.amdhsa_user_sgpr_count 2
		.amdhsa_user_sgpr_dispatch_ptr 0
		.amdhsa_user_sgpr_queue_ptr 0
		.amdhsa_user_sgpr_kernarg_segment_ptr 1
		.amdhsa_user_sgpr_dispatch_id 0
		.amdhsa_user_sgpr_kernarg_preload_length 0
		.amdhsa_user_sgpr_kernarg_preload_offset 0
		.amdhsa_user_sgpr_private_segment_size 0
		.amdhsa_uses_dynamic_stack 0
		.amdhsa_enable_private_segment 0
		.amdhsa_system_sgpr_workgroup_id_x 1
		.amdhsa_system_sgpr_workgroup_id_y 0
		.amdhsa_system_sgpr_workgroup_id_z 0
		.amdhsa_system_sgpr_workgroup_info 0
		.amdhsa_system_vgpr_workitem_id 0
		.amdhsa_next_free_vgpr 256
		.amdhsa_next_free_sgpr 100
		.amdhsa_accum_offset 256
		.amdhsa_reserve_vcc 1
		.amdhsa_float_round_mode_32 0
		.amdhsa_float_round_mode_16_64 0
		.amdhsa_float_denorm_mode_32 3
		.amdhsa_float_denorm_mode_16_64 3
		.amdhsa_dx10_clamp 1
		.amdhsa_ieee_mode 1
		.amdhsa_fp16_overflow 0
		.amdhsa_tg_split 0
		.amdhsa_exception_fp_ieee_invalid_op 0
		.amdhsa_exception_fp_denorm_src 0
		.amdhsa_exception_fp_ieee_div_zero 0
		.amdhsa_exception_fp_ieee_overflow 0
		.amdhsa_exception_fp_ieee_underflow 0
		.amdhsa_exception_fp_ieee_inexact 0
		.amdhsa_exception_int_div_zero 0
	.end_amdhsa_kernel

amdhsa.kernels:
  - .agpr_count:     0
    .args:
      - .offset:         0
        .size:           264
        .value_kind:     by_value
      - .offset:         264
        .size:           4
        .value_kind:     hidden_block_count_x
      - .offset:         268
        .size:           4
        .value_kind:     hidden_block_count_y
      - .offset:         272
        .size:           4
        .value_kind:     hidden_block_count_z
      - .offset:         276
        .size:           2
        .value_kind:     hidden_group_size_x
      - .offset:         278
        .size:           2
        .value_kind:     hidden_group_size_y
      - .offset:         280
        .size:           2
        .value_kind:     hidden_group_size_z
      - .offset:         282
        .size:           2
        .value_kind:     hidden_remainder_x
      - .offset:         284
        .size:           2
        .value_kind:     hidden_remainder_y
      - .offset:         286
        .size:           2
        .value_kind:     hidden_remainder_z
      - .offset:         304
        .size:           8
        .value_kind:     hidden_global_offset_x
      - .offset:         312
        .size:           8
        .value_kind:     hidden_global_offset_y
      - .offset:         320
        .size:           8
        .value_kind:     hidden_global_offset_z
      - .offset:         328
        .size:           2
        .value_kind:     hidden_grid_dims
      - .offset:         384
        .size:           4
        .value_kind:     hidden_dynamic_lds_size
    .group_segment_fixed_size: 0
    .kernarg_segment_align: 8
    .kernarg_segment_size: 520
    .language:       OpenCL C
    .language_version:
      - 2
      - 0
    .max_flat_workgroup_size: 512
    .name:           _Z8mega_fwd4Args
    .private_segment_fixed_size: 0
    .sgpr_count:     106
    .sgpr_spill_count: 93
    .symbol:         _Z8mega_fwd4Args.kd
    .uniform_work_group_size: 1
    .uses_dynamic_stack: false
    .vgpr_count:     256
    .vgpr_spill_count: 0
    .wavefront_size: 64
